# MoE down-projection epilogue: one wait for the loaded row ids/weights before the row blocks instead of a full drain (previous stores included) in front of every block
# speedup vs baseline: 1.0010x; 1.0010x over previous
.LBB0_1363:
	v_mov_b32_e32 v2, v0
	s_nop 15
	s_nop 15
	s_lshl_b32 s23, s23, 8
	v_readfirstlane_b32 s3, v2
	s_ashr_i32 s24, s3, 2
	s_lshr_b32 s3, s3, 1
	s_andn2_b32 s24, s24, 63
	s_and_b32 s3, s3, 0x60
	v_and_or_b32 v35, v2, 15, s24
	s_or_b32 s3, s3, s23
	v_lshrrev_b32_e32 v2, 1, v2
	v_and_or_b32 v18, v2, 24, s3
	s_sub_u32 s3, s20, s43
	s_subb_u32 s23, s21, s44
	s_add_u32 s24, s70, s3
	s_addc_u32 s25, s71, s23
	s_ashr_i32 s23, s22, 31
	s_lshl_b64 s[22:23], s[22:23], 12
	s_add_u32 s22, s67, s22
	s_addc_u32 s23, s33, s23
	s_add_i32 s3, s46, -1
	v_min_i32_e32 v20, s3, v35
	v_ashrrev_i32_e32 v21, 31, v20
	v_ashrrev_i32_e32 v19, 31, v18
	v_lshlrev_b64 v[20:21], 2, v[20:21]
	v_lshl_add_u64 v[6:7], v[18:19], 2, s[22:23]
	v_lshl_add_u64 v[22:23], s[20:21], 0, v[20:21]
	v_lshl_add_u64 v[20:21], s[24:25], 0, v[20:21]
	v_or_b32_e32 v33, 16, v35
	global_load_dwordx4 v[10:13], v[6:7], off offset:16
	global_load_dwordx4 v[14:17], v[6:7], off
	global_load_dwordx4 v[2:5], v[6:7], off offset:528
	s_nop 0
	global_load_dwordx4 v[6:9], v[6:7], off offset:512
	v_or_b32_e32 v31, 32, v35
	global_load_dword v48, v[20:21], off
	v_min_i32_e32 v20, s3, v33
	v_ashrrev_i32_e32 v21, 31, v20
	v_lshlrev_b64 v[20:21], 2, v[20:21]
	global_load_dword v184, v[22:23], off
	v_lshl_add_u64 v[22:23], s[20:21], 0, v[20:21]
	v_lshl_add_u64 v[20:21], s[24:25], 0, v[20:21]
	global_load_dword v44, v[20:21], off
	v_min_i32_e32 v20, s3, v31
	v_ashrrev_i32_e32 v21, 31, v20
	v_lshlrev_b64 v[20:21], 2, v[20:21]
	global_load_dword v46, v[22:23], off
	v_lshl_add_u64 v[22:23], s[20:21], 0, v[20:21]
	v_lshl_add_u64 v[20:21], s[24:25], 0, v[20:21]
	v_or_b32_e32 v29, 48, v35
	global_load_dword v40, v[20:21], off
	v_min_i32_e32 v20, s3, v29
	v_ashrrev_i32_e32 v21, 31, v20
	v_lshlrev_b64 v[20:21], 2, v[20:21]
	global_load_dword v42, v[22:23], off
	v_lshl_add_u64 v[22:23], s[20:21], 0, v[20:21]
	v_lshl_add_u64 v[20:21], s[24:25], 0, v[20:21]
	v_add_u32_e32 v27, 0x80, v35
	global_load_dword v36, v[20:21], off
	v_min_i32_e32 v20, s3, v27
	v_ashrrev_i32_e32 v21, 31, v20
	v_lshlrev_b64 v[20:21], 2, v[20:21]
	global_load_dword v38, v[22:23], off
	v_lshl_add_u64 v[22:23], s[20:21], 0, v[20:21]
	v_lshl_add_u64 v[20:21], s[24:25], 0, v[20:21]
	v_add_u32_e32 v25, 0x90, v35
	global_load_dword v32, v[20:21], off
	v_min_i32_e32 v20, s3, v25
	v_ashrrev_i32_e32 v21, 31, v20
	v_lshlrev_b64 v[20:21], 2, v[20:21]
	global_load_dword v34, v[22:23], off
	v_lshl_add_u64 v[22:23], s[20:21], 0, v[20:21]
	global_load_dword v30, v[22:23], off
	v_lshl_add_u64 v[20:21], s[24:25], 0, v[20:21]
	v_add_u32_e32 v23, 0xa0, v35
	global_load_dword v28, v[20:21], off
	v_min_i32_e32 v20, s3, v23
	v_ashrrev_i32_e32 v21, 31, v20
	v_lshlrev_b64 v[20:21], 2, v[20:21]
	v_lshl_add_u64 v[186:187], s[20:21], 0, v[20:21]
	v_lshl_add_u64 v[20:21], s[24:25], 0, v[20:21]
	global_load_dword v24, v[20:21], off
	v_add_u32_e32 v21, 0xb0, v35
	global_load_dword v26, v[186:187], off
	v_min_i32_e32 v186, s3, v21
	v_ashrrev_i32_e32 v187, 31, v186
	v_lshlrev_b64 v[186:187], 2, v[186:187]
	v_lshl_add_u64 v[188:189], s[20:21], 0, v[186:187]
	v_lshl_add_u64 v[186:187], s[24:25], 0, v[186:187]
	global_load_dword v22, v[188:189], off
	global_load_dword v20, v[186:187], off
	s_waitcnt vmcnt(0)
	v_cmp_gt_i32_e32 vcc, s46, v35
	s_and_saveexec_b64 s[20:21], vcc
	s_mov_b32 s93, 0x84000
	v_readlane_b32 s88, v255, 26
	v_readlane_b32 s62, v255, 33
	s_mov_b64 s[56:57], 0x20000
	v_readlane_b32 s89, v255, 27
	v_readlane_b32 s90, v255, 28
	v_readlane_b32 s91, v255, 29
	s_cbranch_execz .LBB0_1372
	v_ashrrev_i32_e32 v185, 31, v184
	v_lshlrev_b64 v[184:185], 11, v[184:185]
	v_lshl_add_u64 v[184:185], s[14:15], 0, v[184:185]
	v_pk_fma_f32 v[176:177], v[176:177], s[78:79], v[16:17] op_sel_hi:[1,0,1]
	v_pk_fma_f32 v[174:175], v[174:175], s[78:79], v[14:15] op_sel_hi:[1,0,1]
	v_pk_fma_f32 v[172:173], v[172:173], s[78:79], v[12:13] op_sel_hi:[1,0,1]
	v_pk_fma_f32 v[170:171], v[170:171], s[78:79], v[10:11] op_sel_hi:[1,0,1]
	v_lshl_add_u64 v[184:185], v[18:19], 1, v[184:185]
	v_pk_mul_f32 v[176:177], v[176:177], v[48:49] op_sel_hi:[1,0]
	v_pk_mul_f32 v[174:175], v[174:175], v[48:49] op_sel_hi:[1,0]
	v_pk_mul_f32 v[186:187], v[172:173], v[48:49] op_sel_hi:[1,0]
	v_pk_mul_f32 v[172:173], v[170:171], v[48:49] op_sel_hi:[1,0]
	v_cvt_pk_bf16_f32 v170, v174, v175
	v_cvt_pk_bf16_f32 v171, v176, v177
	v_pk_fma_f32 v[168:169], v[168:169], s[78:79], v[8:9] op_sel_hi:[1,0,1]
	v_pk_fma_f32 v[166:167], v[166:167], s[78:79], v[6:7] op_sel_hi:[1,0,1]
	v_pk_fma_f32 v[164:165], v[164:165], s[78:79], v[4:5] op_sel_hi:[1,0,1]
	v_pk_fma_f32 v[162:163], v[162:163], s[78:79], v[2:3] op_sel_hi:[1,0,1]
	v_cvt_pk_bf16_f32 v172, v172, v173
	v_cvt_pk_bf16_f32 v173, v186, v187
	global_store_dwordx4 v[184:185], v[170:173], off
	v_pk_mul_f32 v[168:169], v[168:169], v[48:49] op_sel_hi:[1,0]
	v_pk_mul_f32 v[166:167], v[166:167], v[48:49] op_sel_hi:[1,0]
	v_pk_mul_f32 v[170:171], v[164:165], v[48:49] op_sel_hi:[1,0]
	v_pk_mul_f32 v[48:49], v[162:163], v[48:49] op_sel_hi:[1,0]
	v_cvt_pk_bf16_f32 v162, v166, v167
	v_cvt_pk_bf16_f32 v163, v168, v169
	s_nop 0
	v_cvt_pk_bf16_f32 v164, v48, v49
	v_cvt_pk_bf16_f32 v165, v170, v171
	global_store_dwordx4 v[184:185], v[162:165], off offset:256
	s_or_b64 exec, exec, s[20:21]
	v_cmp_gt_i32_e32 vcc, s46, v33
	s_and_saveexec_b64 s[20:21], vcc
	s_cbranch_execnz .LBB0_1373

.LBB0_1366:
	v_ashrrev_i32_e32 v43, 31, v42
	v_lshlrev_b64 v[42:43], 11, v[42:43]
	v_lshl_add_u64 v[42:43], s[14:15], 0, v[42:43]
	v_lshl_add_u64 v[46:47], v[18:19], 1, v[42:43]
	v_pk_fma_f32 v[42:43], v[144:145], s[78:79], v[16:17] op_sel_hi:[1,0,1]
	v_pk_fma_f32 v[44:45], v[142:143], s[78:79], v[14:15] op_sel_hi:[1,0,1]
	v_pk_mul_f32 v[48:49], v[42:43], v[40:41] op_sel_hi:[1,0]
	v_pk_mul_f32 v[42:43], v[44:45], v[40:41] op_sel_hi:[1,0]
	v_pk_fma_f32 v[44:45], v[140:141], s[78:79], v[12:13] op_sel_hi:[1,0,1]
	v_pk_fma_f32 v[138:139], v[138:139], s[78:79], v[10:11] op_sel_hi:[1,0,1]
	v_pk_mul_f32 v[140:141], v[44:45], v[40:41] op_sel_hi:[1,0]
	v_pk_mul_f32 v[44:45], v[138:139], v[40:41] op_sel_hi:[1,0]
	v_cvt_pk_bf16_f32 v42, v42, v43
	v_cvt_pk_bf16_f32 v43, v48, v49
	v_pk_fma_f32 v[48:49], v[132:133], s[78:79], v[4:5] op_sel_hi:[1,0,1]
	v_cvt_pk_bf16_f32 v44, v44, v45
	v_cvt_pk_bf16_f32 v45, v140, v141
	global_store_dwordx4 v[46:47], v[42:45], off
	v_pk_fma_f32 v[130:131], v[130:131], s[78:79], v[2:3] op_sel_hi:[1,0,1]
	v_pk_mul_f32 v[48:49], v[48:49], v[40:41] op_sel_hi:[1,0]
	v_pk_fma_f32 v[42:43], v[136:137], s[78:79], v[8:9] op_sel_hi:[1,0,1]
	v_pk_fma_f32 v[44:45], v[134:135], s[78:79], v[6:7] op_sel_hi:[1,0,1]
	v_pk_mul_f32 v[42:43], v[42:43], v[40:41] op_sel_hi:[1,0]
	v_pk_mul_f32 v[44:45], v[44:45], v[40:41] op_sel_hi:[1,0]
	v_pk_mul_f32 v[130:131], v[130:131], v[40:41] op_sel_hi:[1,0]
	v_cvt_pk_bf16_f32 v40, v44, v45
	v_cvt_pk_bf16_f32 v41, v42, v43
	s_nop 0
	v_cvt_pk_bf16_f32 v42, v130, v131
	v_cvt_pk_bf16_f32 v43, v48, v49
	global_store_dwordx4 v[46:47], v[40:43], off offset:256
	s_or_b64 exec, exec, s[20:21]
	v_cmp_gt_i32_e32 vcc, s46, v29
	s_and_saveexec_b64 s[20:21], vcc
	s_cbranch_execnz .LBB0_1375

.LBB0_1368:
	v_ashrrev_i32_e32 v35, 31, v34
	v_lshlrev_b64 v[34:35], 11, v[34:35]
	v_lshl_add_u64 v[34:35], s[14:15], 0, v[34:35]
	v_lshl_add_u64 v[38:39], v[18:19], 1, v[34:35]
	v_pk_fma_f32 v[34:35], v[112:113], s[78:79], v[16:17] op_sel_hi:[1,0,1]
	v_pk_fma_f32 v[36:37], v[110:111], s[78:79], v[14:15] op_sel_hi:[1,0,1]
	v_pk_mul_f32 v[40:41], v[34:35], v[32:33] op_sel_hi:[1,0]
	v_pk_mul_f32 v[34:35], v[36:37], v[32:33] op_sel_hi:[1,0]
	v_pk_fma_f32 v[36:37], v[108:109], s[78:79], v[12:13] op_sel_hi:[1,0,1]
	v_pk_fma_f32 v[42:43], v[106:107], s[78:79], v[10:11] op_sel_hi:[1,0,1]
	v_pk_mul_f32 v[44:45], v[36:37], v[32:33] op_sel_hi:[1,0]
	v_pk_mul_f32 v[36:37], v[42:43], v[32:33] op_sel_hi:[1,0]
	v_cvt_pk_bf16_f32 v34, v34, v35
	v_cvt_pk_bf16_f32 v35, v40, v41
	v_pk_fma_f32 v[40:41], v[100:101], s[78:79], v[4:5] op_sel_hi:[1,0,1]
	v_cvt_pk_bf16_f32 v36, v36, v37
	v_cvt_pk_bf16_f32 v37, v44, v45
	global_store_dwordx4 v[38:39], v[34:37], off
	v_pk_fma_f32 v[42:43], v[98:99], s[78:79], v[2:3] op_sel_hi:[1,0,1]
	v_pk_mul_f32 v[40:41], v[40:41], v[32:33] op_sel_hi:[1,0]
	v_pk_fma_f32 v[34:35], v[104:105], s[78:79], v[8:9] op_sel_hi:[1,0,1]
	v_pk_fma_f32 v[36:37], v[102:103], s[78:79], v[6:7] op_sel_hi:[1,0,1]
	v_pk_mul_f32 v[34:35], v[34:35], v[32:33] op_sel_hi:[1,0]
	v_pk_mul_f32 v[36:37], v[36:37], v[32:33] op_sel_hi:[1,0]
	v_pk_mul_f32 v[42:43], v[42:43], v[32:33] op_sel_hi:[1,0]
	v_cvt_pk_bf16_f32 v32, v36, v37
	v_cvt_pk_bf16_f32 v33, v34, v35
	s_nop 0
	v_cvt_pk_bf16_f32 v34, v42, v43
	v_cvt_pk_bf16_f32 v35, v40, v41
	global_store_dwordx4 v[38:39], v[32:35], off offset:256
	s_or_b64 exec, exec, s[20:21]
	v_cmp_gt_i32_e32 vcc, s46, v25
	s_and_saveexec_b64 s[20:21], vcc
	s_cbranch_execnz .LBB0_1377

.LBB0_1370:
	v_ashrrev_i32_e32 v27, 31, v26
	v_lshlrev_b64 v[26:27], 11, v[26:27]
	v_lshl_add_u64 v[26:27], s[14:15], 0, v[26:27]
	v_lshl_add_u64 v[30:31], v[18:19], 1, v[26:27]
	v_pk_fma_f32 v[26:27], v[80:81], s[78:79], v[16:17] op_sel_hi:[1,0,1]
	v_pk_fma_f32 v[28:29], v[78:79], s[78:79], v[14:15] op_sel_hi:[1,0,1]
	v_pk_mul_f32 v[32:33], v[26:27], v[24:25] op_sel_hi:[1,0]
	v_pk_mul_f32 v[26:27], v[28:29], v[24:25] op_sel_hi:[1,0]
	v_pk_fma_f32 v[28:29], v[76:77], s[78:79], v[12:13] op_sel_hi:[1,0,1]
	v_pk_fma_f32 v[34:35], v[74:75], s[78:79], v[10:11] op_sel_hi:[1,0,1]
	v_pk_mul_f32 v[36:37], v[28:29], v[24:25] op_sel_hi:[1,0]
	v_pk_mul_f32 v[28:29], v[34:35], v[24:25] op_sel_hi:[1,0]
	v_cvt_pk_bf16_f32 v26, v26, v27
	v_cvt_pk_bf16_f32 v27, v32, v33
	v_pk_fma_f32 v[32:33], v[68:69], s[78:79], v[4:5] op_sel_hi:[1,0,1]
	v_cvt_pk_bf16_f32 v28, v28, v29
	v_cvt_pk_bf16_f32 v29, v36, v37
	global_store_dwordx4 v[30:31], v[26:29], off
	v_pk_fma_f32 v[34:35], v[66:67], s[78:79], v[2:3] op_sel_hi:[1,0,1]
	v_pk_mul_f32 v[32:33], v[32:33], v[24:25] op_sel_hi:[1,0]
	v_pk_fma_f32 v[26:27], v[72:73], s[78:79], v[8:9] op_sel_hi:[1,0,1]
	v_pk_fma_f32 v[28:29], v[70:71], s[78:79], v[6:7] op_sel_hi:[1,0,1]
	v_pk_mul_f32 v[26:27], v[26:27], v[24:25] op_sel_hi:[1,0]
	v_pk_mul_f32 v[28:29], v[28:29], v[24:25] op_sel_hi:[1,0]
	v_pk_mul_f32 v[34:35], v[34:35], v[24:25] op_sel_hi:[1,0]
	v_cvt_pk_bf16_f32 v24, v28, v29
	v_cvt_pk_bf16_f32 v25, v26, v27
	s_nop 0
	v_cvt_pk_bf16_f32 v26, v34, v35
	v_cvt_pk_bf16_f32 v27, v32, v33
	global_store_dwordx4 v[30:31], v[24:27], off offset:256
	s_or_b64 exec, exec, s[20:21]
	v_cmp_gt_i32_e32 vcc, s46, v21
	s_and_saveexec_b64 s[20:21], vcc
	s_cbranch_execnz .LBB0_1379

.LBB0_1373:
	v_ashrrev_i32_e32 v47, 31, v46
	v_lshlrev_b64 v[46:47], 11, v[46:47]
	v_lshl_add_u64 v[46:47], s[14:15], 0, v[46:47]
	v_lshl_add_u64 v[162:163], v[18:19], 1, v[46:47]
	v_pk_fma_f32 v[46:47], v[160:161], s[78:79], v[16:17] op_sel_hi:[1,0,1]
	v_pk_fma_f32 v[48:49], v[158:159], s[78:79], v[14:15] op_sel_hi:[1,0,1]
	v_pk_mul_f32 v[158:159], v[46:47], v[44:45] op_sel_hi:[1,0]
	v_pk_mul_f32 v[46:47], v[48:49], v[44:45] op_sel_hi:[1,0]
	v_pk_fma_f32 v[48:49], v[156:157], s[78:79], v[12:13] op_sel_hi:[1,0,1]
	v_pk_fma_f32 v[154:155], v[154:155], s[78:79], v[10:11] op_sel_hi:[1,0,1]
	v_pk_mul_f32 v[156:157], v[48:49], v[44:45] op_sel_hi:[1,0]
	v_pk_mul_f32 v[48:49], v[154:155], v[44:45] op_sel_hi:[1,0]
	v_cvt_pk_bf16_f32 v46, v46, v47
	v_cvt_pk_bf16_f32 v47, v158, v159
	v_pk_fma_f32 v[148:149], v[148:149], s[78:79], v[4:5] op_sel_hi:[1,0,1]
	v_cvt_pk_bf16_f32 v48, v48, v49
	v_cvt_pk_bf16_f32 v49, v156, v157
	global_store_dwordx4 v[162:163], v[46:49], off
	v_pk_fma_f32 v[146:147], v[146:147], s[78:79], v[2:3] op_sel_hi:[1,0,1]
	v_pk_mul_f32 v[148:149], v[148:149], v[44:45] op_sel_hi:[1,0]
	v_pk_fma_f32 v[46:47], v[152:153], s[78:79], v[8:9] op_sel_hi:[1,0,1]
	v_pk_fma_f32 v[48:49], v[150:151], s[78:79], v[6:7] op_sel_hi:[1,0,1]
	v_pk_mul_f32 v[46:47], v[46:47], v[44:45] op_sel_hi:[1,0]
	v_pk_mul_f32 v[48:49], v[48:49], v[44:45] op_sel_hi:[1,0]
	v_pk_mul_f32 v[146:147], v[146:147], v[44:45] op_sel_hi:[1,0]
	v_cvt_pk_bf16_f32 v44, v48, v49
	v_cvt_pk_bf16_f32 v45, v46, v47
	s_nop 0
	v_cvt_pk_bf16_f32 v46, v146, v147
	v_cvt_pk_bf16_f32 v47, v148, v149
	global_store_dwordx4 v[162:163], v[44:47], off offset:256
	s_or_b64 exec, exec, s[20:21]
	v_cmp_gt_i32_e32 vcc, s46, v31
	s_and_saveexec_b64 s[20:21], vcc
	s_cbranch_execnz .LBB0_1366

.LBB0_1375:
	v_ashrrev_i32_e32 v39, 31, v38
	v_lshlrev_b64 v[38:39], 11, v[38:39]
	v_lshl_add_u64 v[38:39], s[14:15], 0, v[38:39]
	v_lshl_add_u64 v[42:43], v[18:19], 1, v[38:39]
	v_pk_fma_f32 v[38:39], v[128:129], s[78:79], v[16:17] op_sel_hi:[1,0,1]
	v_pk_fma_f32 v[40:41], v[126:127], s[78:79], v[14:15] op_sel_hi:[1,0,1]
	v_pk_mul_f32 v[44:45], v[38:39], v[36:37] op_sel_hi:[1,0]
	v_pk_mul_f32 v[38:39], v[40:41], v[36:37] op_sel_hi:[1,0]
	v_pk_fma_f32 v[40:41], v[124:125], s[78:79], v[12:13] op_sel_hi:[1,0,1]
	v_pk_fma_f32 v[46:47], v[122:123], s[78:79], v[10:11] op_sel_hi:[1,0,1]
	v_pk_mul_f32 v[48:49], v[40:41], v[36:37] op_sel_hi:[1,0]
	v_pk_mul_f32 v[40:41], v[46:47], v[36:37] op_sel_hi:[1,0]
	v_cvt_pk_bf16_f32 v38, v38, v39
	v_cvt_pk_bf16_f32 v39, v44, v45
	v_pk_fma_f32 v[44:45], v[116:117], s[78:79], v[4:5] op_sel_hi:[1,0,1]
	v_cvt_pk_bf16_f32 v40, v40, v41
	v_cvt_pk_bf16_f32 v41, v48, v49
	global_store_dwordx4 v[42:43], v[38:41], off
	v_pk_fma_f32 v[46:47], v[114:115], s[78:79], v[2:3] op_sel_hi:[1,0,1]
	v_pk_mul_f32 v[44:45], v[44:45], v[36:37] op_sel_hi:[1,0]
	v_pk_fma_f32 v[38:39], v[120:121], s[78:79], v[8:9] op_sel_hi:[1,0,1]
	v_pk_fma_f32 v[40:41], v[118:119], s[78:79], v[6:7] op_sel_hi:[1,0,1]
	v_pk_mul_f32 v[38:39], v[38:39], v[36:37] op_sel_hi:[1,0]
	v_pk_mul_f32 v[40:41], v[40:41], v[36:37] op_sel_hi:[1,0]
	v_pk_mul_f32 v[46:47], v[46:47], v[36:37] op_sel_hi:[1,0]
	v_cvt_pk_bf16_f32 v36, v40, v41
	v_cvt_pk_bf16_f32 v37, v38, v39
	s_nop 0
	v_cvt_pk_bf16_f32 v38, v46, v47
	v_cvt_pk_bf16_f32 v39, v44, v45
	global_store_dwordx4 v[42:43], v[36:39], off offset:256
	s_or_b64 exec, exec, s[20:21]
	v_cmp_gt_i32_e32 vcc, s46, v27
	s_and_saveexec_b64 s[20:21], vcc
	s_cbranch_execnz .LBB0_1368

.LBB0_1377:
	v_ashrrev_i32_e32 v31, 31, v30
	v_lshlrev_b64 v[30:31], 11, v[30:31]
	v_lshl_add_u64 v[30:31], s[14:15], 0, v[30:31]
	v_lshl_add_u64 v[34:35], v[18:19], 1, v[30:31]
	v_pk_fma_f32 v[30:31], v[96:97], s[78:79], v[16:17] op_sel_hi:[1,0,1]
	v_pk_fma_f32 v[32:33], v[94:95], s[78:79], v[14:15] op_sel_hi:[1,0,1]
	v_pk_mul_f32 v[36:37], v[30:31], v[28:29] op_sel_hi:[1,0]
	v_pk_mul_f32 v[30:31], v[32:33], v[28:29] op_sel_hi:[1,0]
	v_pk_fma_f32 v[32:33], v[92:93], s[78:79], v[12:13] op_sel_hi:[1,0,1]
	v_pk_fma_f32 v[38:39], v[90:91], s[78:79], v[10:11] op_sel_hi:[1,0,1]
	v_pk_mul_f32 v[40:41], v[32:33], v[28:29] op_sel_hi:[1,0]
	v_pk_mul_f32 v[32:33], v[38:39], v[28:29] op_sel_hi:[1,0]
	v_cvt_pk_bf16_f32 v30, v30, v31
	v_cvt_pk_bf16_f32 v31, v36, v37
	v_pk_fma_f32 v[36:37], v[84:85], s[78:79], v[4:5] op_sel_hi:[1,0,1]
	v_cvt_pk_bf16_f32 v32, v32, v33
	v_cvt_pk_bf16_f32 v33, v40, v41
	global_store_dwordx4 v[34:35], v[30:33], off
	v_pk_fma_f32 v[38:39], v[82:83], s[78:79], v[2:3] op_sel_hi:[1,0,1]
	v_pk_mul_f32 v[36:37], v[36:37], v[28:29] op_sel_hi:[1,0]
	v_pk_fma_f32 v[30:31], v[88:89], s[78:79], v[8:9] op_sel_hi:[1,0,1]
	v_pk_fma_f32 v[32:33], v[86:87], s[78:79], v[6:7] op_sel_hi:[1,0,1]
	v_pk_mul_f32 v[30:31], v[30:31], v[28:29] op_sel_hi:[1,0]
	v_pk_mul_f32 v[32:33], v[32:33], v[28:29] op_sel_hi:[1,0]
	v_pk_mul_f32 v[38:39], v[38:39], v[28:29] op_sel_hi:[1,0]
	v_cvt_pk_bf16_f32 v28, v32, v33
	v_cvt_pk_bf16_f32 v29, v30, v31
	s_nop 0
	v_cvt_pk_bf16_f32 v30, v38, v39
	v_cvt_pk_bf16_f32 v31, v36, v37
	global_store_dwordx4 v[34:35], v[28:31], off offset:256
	s_or_b64 exec, exec, s[20:21]
	v_cmp_gt_i32_e32 vcc, s46, v23
	s_and_saveexec_b64 s[20:21], vcc
	s_cbranch_execnz .LBB0_1370

.LBB0_1379:
	v_ashrrev_i32_e32 v23, 31, v22
	v_lshlrev_b64 v[22:23], 11, v[22:23]
	v_lshl_add_u64 v[22:23], s[14:15], 0, v[22:23]
	v_pk_fma_f32 v[16:17], v[64:65], s[78:79], v[16:17] op_sel_hi:[1,0,1]
	v_pk_fma_f32 v[14:15], v[62:63], s[78:79], v[14:15] op_sel_hi:[1,0,1]
	v_pk_fma_f32 v[12:13], v[60:61], s[78:79], v[12:13] op_sel_hi:[1,0,1]
	v_pk_fma_f32 v[10:11], v[58:59], s[78:79], v[10:11] op_sel_hi:[1,0,1]
	v_lshl_add_u64 v[18:19], v[18:19], 1, v[22:23]
	v_pk_mul_f32 v[16:17], v[16:17], v[20:21] op_sel_hi:[1,0]
	v_pk_mul_f32 v[14:15], v[14:15], v[20:21] op_sel_hi:[1,0]
	v_pk_mul_f32 v[22:23], v[12:13], v[20:21] op_sel_hi:[1,0]
	v_pk_mul_f32 v[12:13], v[10:11], v[20:21] op_sel_hi:[1,0]
	v_cvt_pk_bf16_f32 v10, v14, v15
	v_cvt_pk_bf16_f32 v11, v16, v17
	v_pk_fma_f32 v[4:5], v[52:53], s[78:79], v[4:5] op_sel_hi:[1,0,1]
	v_pk_fma_f32 v[2:3], v[50:51], s[78:79], v[2:3] op_sel_hi:[1,0,1]
	v_cvt_pk_bf16_f32 v12, v12, v13
	v_cvt_pk_bf16_f32 v13, v22, v23
	global_store_dwordx4 v[18:19], v[10:13], off
	v_pk_fma_f32 v[8:9], v[56:57], s[78:79], v[8:9] op_sel_hi:[1,0,1]
	v_pk_fma_f32 v[6:7], v[54:55], s[78:79], v[6:7] op_sel_hi:[1,0,1]
	v_pk_mul_f32 v[10:11], v[4:5], v[20:21] op_sel_hi:[1,0]
	v_pk_mul_f32 v[4:5], v[2:3], v[20:21] op_sel_hi:[1,0]
	v_pk_mul_f32 v[8:9], v[8:9], v[20:21] op_sel_hi:[1,0]
	v_pk_mul_f32 v[6:7], v[6:7], v[20:21] op_sel_hi:[1,0]
	s_nop 0
	v_cvt_pk_bf16_f32 v2, v6, v7
	v_cvt_pk_bf16_f32 v3, v8, v9
	v_cvt_pk_bf16_f32 v4, v4, v5
	v_cvt_pk_bf16_f32 v5, v10, v11
	global_store_dwordx4 v[18:19], v[2:5], off offset:256
	s_or_b64 exec, exec, s[20:21]
	s_andn2_b64 vcc, exec, s[18:19]
	s_mov_b64 s[18:19], -1
	s_cbranch_vccnz .LBB0_1349
